# v19 + MLA: next block's Q fragments requested with its first K/V tiles at the end of this block's main loop; prefetched blocks skip their own Q loads
# baseline (speedup 1.0000x reference)
.LBB0_939:
	v_mov_b32_e32 v194, v0
	s_or_b64 s[22:23], s[4:5], s[68:69]
	v_readfirstlane_b32 s0, v194
	s_ashr_i32 s18, s0, 6
	s_and_b64 s[12:13], s[2:3], exec
	s_cselect_b32 s1, s76, s77
	s_lshl_b32 s35, s18, 5
	s_or_b32 s12, s26, s1
	s_ashr_i32 s13, s35, 31
	s_add_u32 s12, s12, s35
	s_addc_u32 s13, s27, s13
	s_mul_i32 s16, s13, 0xc00
	s_mul_hi_u32 s17, s12, 0xc00
	v_and_b32_e32 v195, 31, v194
	v_bfe_u32 v196, v194, 5, 1
	s_add_i32 s17, s17, s16
	s_mul_i32 s16, s12, 0xc00
	s_add_u32 s16, s72, s16
	v_lshlrev_b32_e32 v20, 4, v196
	v_mul_u32_u24_e32 v1, 0xc00, v195
	s_addc_u32 s17, s73, s17
	v_or_b32_e32 v1, v20, v1
	s_and_b64 vcc, exec, s[22:23]
	s_cbranch_vccnz .Lmla_q_pre
	global_load_dwordx4 v[130:133], v1, s[16:17]
	global_load_dwordx4 v[134:137], v1, s[16:17] offset:32
	global_load_dwordx4 v[138:141], v1, s[16:17] offset:64
	global_load_dwordx4 v[142:145], v1, s[16:17] offset:96
	global_load_dwordx4 v[146:149], v1, s[16:17] offset:128
	global_load_dwordx4 v[150:153], v1, s[16:17] offset:160
	global_load_dwordx4 v[154:157], v1, s[16:17] offset:192
	global_load_dwordx4 v[158:161], v1, s[16:17] offset:224
	global_load_dwordx4 v[162:165], v1, s[16:17] offset:256
	global_load_dwordx4 v[166:169], v1, s[16:17] offset:288
	global_load_dwordx4 v[170:173], v1, s[16:17] offset:320
	global_load_dwordx4 v[174:177], v1, s[16:17] offset:352
.Lmla_q_pre:
	s_lshl_b32 s16, s18, 3
	s_waitcnt lgkmcnt(0)
	v_bfe_u32 v3, v194, 2, 3
	v_mov_b32_e32 v4, 0xffff3
	v_bitop3_b32 v3, s16, v4, v3 bitop3:0xc8
	v_lshrrev_b32_e32 v4, 1, v194
	s_lshl_b32 s17, s18, 2
	v_bfe_u32 v1, v194, 4, 2
	v_lshlrev_b32_e32 v21, 4, v194
	v_and_b32_e32 v4, 8, v4
	s_and_b32 s17, s17, 4
	v_and_b32_e32 v6, 48, v194
	s_movk_i32 s19, 0xf0
	v_or3_b32 v3, v4, v3, s17
	s_lshl_b32 s17, s18, 15
	v_lshlrev_b32_e32 v5, 12, v1
	v_bitop3_b32 v6, v21, v6, s19 bitop3:0x6c
	s_lshl_b32 s21, s18, 7
	s_and_b32 s21, s21, 0x80
	v_xor_b32_e32 v6, s21, v6
	v_and_b32_e32 v4, 48, v21
	v_lshlrev_b32_e32 v3, 12, v3
	v_or3_b32 v198, s17, v5, v6
	v_lshlrev_b32_e32 v5, 6, v196
	v_or3_b32 v1, v1, s16, 4
	v_or3_b32 v3, v3, v4, v5
	v_lshlrev_b32_e32 v4, 12, v1
	v_lshlrev_b32_e32 v1, 4, v1
	v_and_b32_e32 v2, 0xf0, v21
	v_and_b32_e32 v1, 0xf0, v1
	v_bitop3_b32 v200, v1, v4, v2 bitop3:0xde
	v_bfe_u32 v1, v194, 3, 3
	v_lshlrev_b32_e32 v2, 7, v1
	v_bfe_u32 v4, v194, 4, 2
	s_and_b32 s21, s18, 1
	s_lshl_b32 s21, s21, 2
	v_or_b32_e32 v4, s21, v4
	v_bitop3_b32 v1, v4, v194, 7 bitop3:0x78
	s_lshl_b32 s16, s18, 10
	v_lshlrev_b32_e32 v1, 4, v1
	s_lshl_b32 s17, s18, 11
	v_or3_b32 v201, v1, v2, s16
	s_add_i32 s17, s17, 0
	s_add_i32 s16, s16, 0
	v_or_b32_e32 v197, 0x100, v3
	v_or_b32_e32 v199, 0x180, v3
	s_add_i32 s19, s17, 0xc000
	s_add_i32 s18, s16, 0x18000
	s_and_b64 vcc, exec, s[22:23]
	s_cbranch_vccnz .LBB0_941
	s_mov_b32 m0, s19
	s_nop 0
	global_load_lds_dwordx4 v198, s[38:39]
	s_add_i32 s21, s17, 0xc400
	s_mov_b32 m0, s21
	s_nop 0
	global_load_lds_dwordx4 v200, s[38:39]
	s_mov_b32 m0, s17
	s_nop 0
	global_load_lds_dwordx4 v197, s[38:39]
	s_add_i32 s21, s17, 0x400
	s_mov_b32 m0, s21
	s_nop 0
	global_load_lds_dwordx4 v199, s[38:39]
	s_mov_b32 m0, s18
	s_nop 0
	global_load_lds_dwordx4 v201, s[56:57]
	s_add_i32 s21, s17, 0x10000
	s_mov_b32 m0, s21
	s_nop 0
	global_load_lds_dwordx4 v198, s[58:59]
	s_add_i32 s21, s17, 0x10400
	s_mov_b32 m0, s21
	s_nop 0
	global_load_lds_dwordx4 v200, s[58:59]
	s_add_i32 s21, s17, 0x4000
	s_mov_b32 m0, s21
	s_nop 0
	global_load_lds_dwordx4 v197, s[58:59]
	s_add_i32 s21, s17, 0x4400
	s_mov_b32 m0, s21
	s_nop 0
	global_load_lds_dwordx4 v199, s[58:59]
	s_add_i32 s21, s16, 0x1a000
	s_mov_b32 m0, s21
	s_nop 0
	global_load_lds_dwordx4 v201, s[60:61]

.LBB0_964:
	s_xor_b64 s[0:1], s[68:69], -1
	s_or_b64 s[0:1], s[0:1], s[8:9]
	s_and_b64 vcc, exec, s[0:1]
	s_cbranch_vccz .LBB0_966
	s_lshl_b32 s98, s24, 8
	s_and_b32 s98, s98, 0x300
	s_and_b64 s[0:1], s[68:69], s[8:9]
	s_and_b64 s[0:1], s[0:1], exec
	s_cselect_b32 s21, s71, s70
	s_cselect_b32 s98, s98, s77
	s_ashr_i32 s99, s21, 3
	s_lshl_b32 s99, s99, 11
	s_or_b32 s99, s99, s98
	v_readfirstlane_b32 s0, v0
	s_nop 3
	s_ashr_i32 s0, s0, 6
	s_lshl_b32 s0, s0, 5
	s_add_i32 s99, s99, s0
	s_mul_hi_u32 s101, s99, 0xc00
	s_mul_i32 s100, s99, 0xc00
	s_and_b32 s0, s21, 7
	s_mul_i32 s0, s0, 0x180
	v_readlane_b32 s98, v251, 52
	v_readlane_b32 s99, v251, 53
	s_nop 3
	s_add_u32 s98, s98, s0
	s_addc_u32 s99, s99, 0
	s_add_u32 s100, s100, s98
	s_addc_u32 s101, s101, s99
	v_and_b32_e32 v128, 31, v0
	v_mul_u32_u24_e32 v128, 0xc00, v128
	v_bfe_u32 v129, v0, 5, 1
	v_lshl_or_b32 v128, v129, 4, v128
	global_load_dwordx4 v[130:133], v128, s[100:101]
	global_load_dwordx4 v[134:137], v128, s[100:101] offset:32
	global_load_dwordx4 v[138:141], v128, s[100:101] offset:64
	global_load_dwordx4 v[142:145], v128, s[100:101] offset:96
	global_load_dwordx4 v[146:149], v128, s[100:101] offset:128
	global_load_dwordx4 v[150:153], v128, s[100:101] offset:160
	global_load_dwordx4 v[154:157], v128, s[100:101] offset:192
	global_load_dwordx4 v[158:161], v128, s[100:101] offset:224
	global_load_dwordx4 v[162:165], v128, s[100:101] offset:256
	global_load_dwordx4 v[166:169], v128, s[100:101] offset:288
	global_load_dwordx4 v[170:173], v128, s[100:101] offset:320
	global_load_dwordx4 v[174:177], v128, s[100:101] offset:352
	v_readlane_b32 s40, v249, 7
	s_ashr_i32 s0, s21, 3
	v_readlane_b32 s41, v249, 8
	v_readlane_b32 s42, v249, 9
	v_readlane_b32 s43, v249, 10
	v_readlane_b32 s44, v249, 11
	v_readlane_b32 s45, v249, 12
	s_ashr_i32 s1, s0, 31
	v_readlane_b32 s46, v249, 13
	v_readlane_b32 s47, v249, 14
	s_mov_b64 s[40:41], s[44:45]
	s_lshl_b64 s[22:23], s[0:1], 23
	s_mov_b64 s[42:43], s[46:47]
	s_add_u32 s22, s42, s22
	s_addc_u32 s23, s43, s23
	s_lshl_b32 s21, s21, 9
	s_and_b32 s21, s21, 0xe00
	s_add_u32 s22, s22, s21
	s_addc_u32 s23, s23, 0
	s_lshl_b64 s[0:1], s[0:1], 18
	v_readlane_b32 s21, v251, 40
	s_add_u32 s0, s21, s0
	v_readlane_b32 s21, v251, 41
	s_mov_b32 m0, s19
	s_nop 0
	global_load_lds_dwordx4 v198, s[22:23]
	s_addc_u32 s1, s21, s1
	s_add_i32 s19, s17, 0xc400
	s_mov_b32 m0, s19
	s_nop 0
	global_load_lds_dwordx4 v200, s[22:23]
	s_mov_b32 m0, s17
	s_nop 0
	global_load_lds_dwordx4 v197, s[22:23]
	s_add_i32 s19, s17, 0x400
	s_mov_b32 m0, s19
	s_nop 0
	global_load_lds_dwordx4 v199, s[22:23]
	s_mov_b32 m0, s18
	s_nop 0
	global_load_lds_dwordx4 v201, s[0:1]
	s_add_u32 s18, s22, 0x40000
	s_addc_u32 s19, s23, 0
	s_add_u32 s0, s0, 0x2000
	s_addc_u32 s1, s1, 0
	s_add_i32 s21, s17, 0x10000
	s_mov_b32 m0, s21
	s_nop 0
	global_load_lds_dwordx4 v198, s[18:19]
	s_add_i32 s21, s17, 0x10400
	s_mov_b32 m0, s21
	s_nop 0
	global_load_lds_dwordx4 v200, s[18:19]
	s_add_i32 s21, s17, 0x4000
	s_mov_b32 m0, s21
	s_nop 0
	global_load_lds_dwordx4 v197, s[18:19]
	s_addk_i32 s17, 0x4400
	s_mov_b32 m0, s17
	s_nop 0
	global_load_lds_dwordx4 v199, s[18:19]
	s_add_i32 s16, s16, 0x1a000
	s_mov_b32 m0, s16
	s_nop 0
	global_load_lds_dwordx4 v201, s[0:1]
